# combination: v6 + hook loads without nt + L2 touch prefetch in the P6a/P6b/P7 epilogues
# baseline (speedup 1.0000x reference)
.LBB0_1112:
	ds_read_b128 v[0:3], v191
	ds_read_b128 v[4:7], v195
	ds_read_b128 v[8:11], v196
	ds_read_b128 v[12:15], v197
	s_add_u32 s36, s34, 0x80
	s_addc_u32 s37, s35, 0
	s_cmp_eq_u32 s62, 12
	s_cselect_b32 s39, s21, s37
	s_cselect_b32 s38, s58, s36
	s_cselect_b32 s37, s23, s61
	s_cselect_b32 s36, s59, s60
	v_lshl_add_u64 v[144:145], s[34:35], 0, v[166:167]
	s_add_i32 m0, s43, 0xc000
	ds_read_b128 v[168:171], v208
	ds_read_b128 v[172:175], v208 offset:1024
	ds_read_b128 v[176:179], v208 offset:2048
	ds_read_b128 v[180:183], v208 offset:3072
	ds_read_b128 v[212:215], v208 offset:4096
	ds_read_b128 v[216:219], v208 offset:5120
	ds_read_b128 v[220:223], v208 offset:6144
	ds_read_b128 v[224:227], v208 offset:7168
	global_load_lds_dwordx4 v[144:145], off
	v_lshl_add_u64 v[144:145], s[34:35], 0, v[164:165]
	s_add_i32 m0, s43, 0xe000
	s_nop 0
	global_load_lds_dwordx4 v[144:145], off
	s_waitcnt lgkmcnt(8)
	s_barrier
	s_waitcnt lgkmcnt(0)
	s_setprio 1
	s_waitcnt lgkmcnt(0)
	v_mfma_scale_f32_16x16x128_f8f6f4 v[140:143], v[0:7], v[168:175], v[140:143], v209, v210 op_sel_hi:[0,0,0]
	v_mfma_scale_f32_16x16x128_f8f6f4 v[136:139], v[8:15], v[168:175], v[136:139], v209, v210 op_sel_hi:[0,0,0]
	v_mfma_scale_f32_16x16x128_f8f6f4 v[132:135], v[0:7], v[176:183], v[132:135], v209, v210 op_sel_hi:[0,0,0]
	v_mfma_scale_f32_16x16x128_f8f6f4 v[128:131], v[8:15], v[176:183], v[128:131], v209, v210 op_sel_hi:[0,0,0]
	v_mfma_scale_f32_16x16x128_f8f6f4 v[124:127], v[0:7], v[212:219], v[124:127], v209, v210 op_sel_hi:[0,0,0]
	v_mfma_scale_f32_16x16x128_f8f6f4 v[120:123], v[8:15], v[212:219], v[120:123], v209, v210 op_sel_hi:[0,0,0]
	v_mfma_scale_f32_16x16x128_f8f6f4 v[116:119], v[0:7], v[220:227], v[116:119], v209, v210 op_sel_hi:[0,0,0]
	v_mfma_scale_f32_16x16x128_f8f6f4 v[112:115], v[8:15], v[220:227], v[112:115], v209, v210 op_sel_hi:[0,0,0]
	s_setprio 0
	s_barrier
	s_mov_b32 m0, s44
	v_lshl_add_u64 v[144:145], s[36:37], 0, v[152:153]
	ds_read_b128 v[228:231], v192
	ds_read_b128 v[232:235], v198
	ds_read_b128 v[236:239], v199
	ds_read_b128 v[240:243], v200
	global_load_lds_dwordx4 v[144:145], off
	v_lshl_add_u64 v[146:147], s[36:37], 0, v[154:155]
	s_mov_b32 m0, s45
	s_nop 0
	global_load_lds_dwordx4 v[146:147], off
	s_barrier
	s_waitcnt lgkmcnt(0)
	s_setprio 1
	s_waitcnt lgkmcnt(0)
	v_mfma_scale_f32_16x16x128_f8f6f4 v[76:79], v[228:235], v[168:175], v[76:79], v209, v210 op_sel_hi:[0,0,0]
	v_mfma_scale_f32_16x16x128_f8f6f4 v[72:75], v[236:243], v[168:175], v[72:75], v209, v210 op_sel_hi:[0,0,0]
	v_mfma_scale_f32_16x16x128_f8f6f4 v[68:71], v[228:235], v[176:183], v[68:71], v209, v210 op_sel_hi:[0,0,0]
	v_mfma_scale_f32_16x16x128_f8f6f4 v[64:67], v[236:243], v[176:183], v[64:67], v209, v210 op_sel_hi:[0,0,0]
	v_mfma_scale_f32_16x16x128_f8f6f4 v[60:63], v[228:235], v[212:219], v[60:63], v209, v210 op_sel_hi:[0,0,0]
	v_mfma_scale_f32_16x16x128_f8f6f4 v[56:59], v[236:243], v[212:219], v[56:59], v209, v210 op_sel_hi:[0,0,0]
	v_mfma_scale_f32_16x16x128_f8f6f4 v[52:55], v[228:235], v[220:227], v[52:55], v209, v210 op_sel_hi:[0,0,0]
	v_mfma_scale_f32_16x16x128_f8f6f4 v[48:51], v[236:243], v[220:227], v[48:51], v209, v210 op_sel_hi:[0,0,0]
	s_setprio 0
	s_mov_b32 m0, s43
	v_lshl_add_u64 v[148:149], s[38:39], 0, v[156:157]
	s_barrier
	ds_read_b128 v[168:171], v208 offset:16384
	ds_read_b128 v[172:175], v208 offset:17408
	ds_read_b128 v[176:179], v208 offset:18432
	ds_read_b128 v[180:183], v208 offset:19456
	ds_read_b128 v[212:215], v208 offset:20480
	ds_read_b128 v[216:219], v208 offset:21504
	ds_read_b128 v[220:223], v208 offset:22528
	ds_read_b128 v[224:227], v208 offset:23552
	global_load_lds_dwordx4 v[148:149], off
	v_lshl_add_u64 v[150:151], s[38:39], 0, v[158:159]
	s_mov_b32 m0, s46
	s_nop 0
	global_load_lds_dwordx4 v[150:151], off
	s_barrier
	s_waitcnt lgkmcnt(0)
	s_setprio 1
	s_waitcnt lgkmcnt(0)
	v_mfma_scale_f32_16x16x128_f8f6f4 v[108:111], v[0:7], v[168:175], v[108:111], v209, v210 op_sel_hi:[0,0,0]
	v_mfma_scale_f32_16x16x128_f8f6f4 v[104:107], v[8:15], v[168:175], v[104:107], v209, v210 op_sel_hi:[0,0,0]
	v_mfma_scale_f32_16x16x128_f8f6f4 v[100:103], v[0:7], v[176:183], v[100:103], v209, v210 op_sel_hi:[0,0,0]
	v_mfma_scale_f32_16x16x128_f8f6f4 v[96:99], v[8:15], v[176:183], v[96:99], v209, v210 op_sel_hi:[0,0,0]
	v_mfma_scale_f32_16x16x128_f8f6f4 v[92:95], v[0:7], v[212:219], v[92:95], v209, v210 op_sel_hi:[0,0,0]
	v_mfma_scale_f32_16x16x128_f8f6f4 v[88:91], v[8:15], v[212:219], v[88:91], v209, v210 op_sel_hi:[0,0,0]
	v_mfma_scale_f32_16x16x128_f8f6f4 v[84:87], v[0:7], v[220:227], v[84:87], v209, v210 op_sel_hi:[0,0,0]
	v_mfma_scale_f32_16x16x128_f8f6f4 v[80:83], v[8:15], v[220:227], v[80:83], v209, v210 op_sel_hi:[0,0,0]
	s_setprio 0
	s_barrier
	s_add_u32 s64, s36, 0x40000
	s_addc_u32 s65, s37, 0
	s_mov_b32 m0, s47
	v_lshl_add_u64 v[0:1], s[64:65], 0, v[152:153]
	global_load_lds_dwordx4 v[0:1], off
	v_lshl_add_u64 v[0:1], s[64:65], 0, v[154:155]
	s_mov_b32 m0, s48
	s_nop 0
	global_load_lds_dwordx4 v[0:1], off
	s_waitcnt vmcnt(6)
	s_barrier
	s_setprio 1
	v_mfma_scale_f32_16x16x128_f8f6f4 v[44:47], v[228:235], v[168:175], v[44:47], v209, v210 op_sel_hi:[0,0,0]
	v_mfma_scale_f32_16x16x128_f8f6f4 v[40:43], v[236:243], v[168:175], v[40:43], v209, v210 op_sel_hi:[0,0,0]
	v_mfma_scale_f32_16x16x128_f8f6f4 v[36:39], v[228:235], v[176:183], v[36:39], v209, v210 op_sel_hi:[0,0,0]
	v_mfma_scale_f32_16x16x128_f8f6f4 v[32:35], v[236:243], v[176:183], v[32:35], v209, v210 op_sel_hi:[0,0,0]
	v_mfma_scale_f32_16x16x128_f8f6f4 v[28:31], v[228:235], v[212:219], v[28:31], v209, v210 op_sel_hi:[0,0,0]
	v_mfma_scale_f32_16x16x128_f8f6f4 v[24:27], v[236:243], v[212:219], v[24:27], v209, v210 op_sel_hi:[0,0,0]
	v_mfma_scale_f32_16x16x128_f8f6f4 v[20:23], v[228:235], v[220:227], v[20:23], v209, v210 op_sel_hi:[0,0,0]
	v_mfma_scale_f32_16x16x128_f8f6f4 v[16:19], v[236:243], v[220:227], v[16:19], v209, v210 op_sel_hi:[0,0,0]
	s_setprio 0
	s_barrier
	ds_read_b128 v[0:3], v193
	ds_read_b128 v[4:7], v201
	ds_read_b128 v[8:11], v202
	ds_read_b128 v[12:15], v203
	s_mov_b32 m0, s49
	v_lshl_add_u64 v[184:185], s[38:39], 0, v[160:161]
	ds_read_b128 v[168:171], v208 offset:32768
	ds_read_b128 v[172:175], v208 offset:33792
	ds_read_b128 v[176:179], v208 offset:34816
	ds_read_b128 v[180:183], v208 offset:35840
	ds_read_b128 v[212:215], v208 offset:36864
	ds_read_b128 v[216:219], v208 offset:37888
	ds_read_b128 v[220:223], v208 offset:38912
	ds_read_b128 v[224:227], v208 offset:39936
	global_load_lds_dwordx4 v[184:185], off
	v_lshl_add_u64 v[184:185], s[38:39], 0, v[162:163]
	s_mov_b32 m0, s50
	s_nop 0
	global_load_lds_dwordx4 v[184:185], off
	s_waitcnt lgkmcnt(8)
	s_barrier
	s_waitcnt lgkmcnt(0)
	s_setprio 1
	s_waitcnt lgkmcnt(0)
	v_mfma_scale_f32_16x16x128_f8f6f4 v[140:143], v[0:7], v[168:175], v[140:143], v209, v210 op_sel_hi:[0,0,0]
	v_mfma_scale_f32_16x16x128_f8f6f4 v[136:139], v[8:15], v[168:175], v[136:139], v209, v210 op_sel_hi:[0,0,0]
	v_mfma_scale_f32_16x16x128_f8f6f4 v[132:135], v[0:7], v[176:183], v[132:135], v209, v210 op_sel_hi:[0,0,0]
	v_mfma_scale_f32_16x16x128_f8f6f4 v[128:131], v[8:15], v[176:183], v[128:131], v209, v210 op_sel_hi:[0,0,0]
	v_mfma_scale_f32_16x16x128_f8f6f4 v[124:127], v[0:7], v[212:219], v[124:127], v209, v210 op_sel_hi:[0,0,0]
	v_mfma_scale_f32_16x16x128_f8f6f4 v[120:123], v[8:15], v[212:219], v[120:123], v209, v210 op_sel_hi:[0,0,0]
	v_mfma_scale_f32_16x16x128_f8f6f4 v[116:119], v[0:7], v[220:227], v[116:119], v209, v210 op_sel_hi:[0,0,0]
	v_mfma_scale_f32_16x16x128_f8f6f4 v[112:115], v[8:15], v[220:227], v[112:115], v209, v210 op_sel_hi:[0,0,0]
	s_setprio 0
	s_barrier
	s_mov_b32 m0, s52
	v_lshl_add_u64 v[144:145], v[144:145], 0, s[16:17]
	ds_read_b128 v[228:231], v194
	ds_read_b128 v[232:235], v204
	ds_read_b128 v[236:239], v205
	ds_read_b128 v[240:243], v206
	global_load_lds_dwordx4 v[144:145], off
	v_lshl_add_u64 v[144:145], v[146:147], 0, s[16:17]
	s_mov_b32 m0, s53
	s_nop 0
	global_load_lds_dwordx4 v[144:145], off
	s_barrier
	s_waitcnt lgkmcnt(0)
	s_setprio 1
	s_waitcnt lgkmcnt(0)
	v_mfma_scale_f32_16x16x128_f8f6f4 v[76:79], v[228:235], v[168:175], v[76:79], v209, v210 op_sel_hi:[0,0,0]
	v_mfma_scale_f32_16x16x128_f8f6f4 v[72:75], v[236:243], v[168:175], v[72:75], v209, v210 op_sel_hi:[0,0,0]
	v_mfma_scale_f32_16x16x128_f8f6f4 v[68:71], v[228:235], v[176:183], v[68:71], v209, v210 op_sel_hi:[0,0,0]
	v_mfma_scale_f32_16x16x128_f8f6f4 v[64:67], v[236:243], v[176:183], v[64:67], v209, v210 op_sel_hi:[0,0,0]
	v_mfma_scale_f32_16x16x128_f8f6f4 v[60:63], v[228:235], v[212:219], v[60:63], v209, v210 op_sel_hi:[0,0,0]
	v_mfma_scale_f32_16x16x128_f8f6f4 v[56:59], v[236:243], v[212:219], v[56:59], v209, v210 op_sel_hi:[0,0,0]
	v_mfma_scale_f32_16x16x128_f8f6f4 v[52:55], v[228:235], v[220:227], v[52:55], v209, v210 op_sel_hi:[0,0,0]
	v_mfma_scale_f32_16x16x128_f8f6f4 v[48:51], v[236:243], v[220:227], v[48:51], v209, v210 op_sel_hi:[0,0,0]
	s_setprio 0
	s_mov_b32 m0, s54
	v_lshl_add_u64 v[144:145], v[148:149], 0, s[16:17]
	s_barrier
	ds_read_b128 v[168:171], v208 offset:49152
	ds_read_b128 v[172:175], v208 offset:50176
	ds_read_b128 v[176:179], v208 offset:51200
	ds_read_b128 v[180:183], v208 offset:52224
	ds_read_b128 v[212:215], v208 offset:53248
	ds_read_b128 v[216:219], v208 offset:54272
	ds_read_b128 v[220:223], v208 offset:55296
	ds_read_b128 v[224:227], v208 offset:56320
	global_load_lds_dwordx4 v[144:145], off
	v_lshl_add_u64 v[144:145], v[150:151], 0, s[16:17]
	s_mov_b32 m0, s55
	s_nop 0
	global_load_lds_dwordx4 v[144:145], off
	s_barrier
	s_waitcnt lgkmcnt(0)
	s_setprio 1
	s_waitcnt lgkmcnt(0)
	v_mfma_scale_f32_16x16x128_f8f6f4 v[108:111], v[0:7], v[168:175], v[108:111], v209, v210 op_sel_hi:[0,0,0]
	v_mfma_scale_f32_16x16x128_f8f6f4 v[104:107], v[8:15], v[168:175], v[104:107], v209, v210 op_sel_hi:[0,0,0]
	v_mfma_scale_f32_16x16x128_f8f6f4 v[100:103], v[0:7], v[176:183], v[100:103], v209, v210 op_sel_hi:[0,0,0]
	v_mfma_scale_f32_16x16x128_f8f6f4 v[96:99], v[8:15], v[176:183], v[96:99], v209, v210 op_sel_hi:[0,0,0]
	v_mfma_scale_f32_16x16x128_f8f6f4 v[92:95], v[0:7], v[212:219], v[92:95], v209, v210 op_sel_hi:[0,0,0]
	v_mfma_scale_f32_16x16x128_f8f6f4 v[88:91], v[8:15], v[212:219], v[88:91], v209, v210 op_sel_hi:[0,0,0]
	v_mfma_scale_f32_16x16x128_f8f6f4 v[84:87], v[0:7], v[220:227], v[84:87], v209, v210 op_sel_hi:[0,0,0]
	v_mfma_scale_f32_16x16x128_f8f6f4 v[80:83], v[8:15], v[220:227], v[80:83], v209, v210 op_sel_hi:[0,0,0]
	s_setprio 0
	s_barrier
	s_add_u32 s36, s36, 0x40080
	s_addc_u32 s37, s37, 0
	s_mov_b32 m0, s56
	v_lshl_add_u64 v[0:1], s[36:37], 0, v[152:153]
	global_load_lds_dwordx4 v[0:1], off
	v_lshl_add_u64 v[0:1], s[36:37], 0, v[154:155]
	s_mov_b32 m0, s57
	s_nop 0
	global_load_lds_dwordx4 v[0:1], off
	s_waitcnt vmcnt(6)
	s_barrier
	s_setprio 1
	v_mfma_scale_f32_16x16x128_f8f6f4 v[44:47], v[228:235], v[168:175], v[44:47], v209, v210 op_sel_hi:[0,0,0]
	v_mfma_scale_f32_16x16x128_f8f6f4 v[40:43], v[236:243], v[168:175], v[40:43], v209, v210 op_sel_hi:[0,0,0]
	v_mfma_scale_f32_16x16x128_f8f6f4 v[36:39], v[228:235], v[176:183], v[36:39], v209, v210 op_sel_hi:[0,0,0]
	v_mfma_scale_f32_16x16x128_f8f6f4 v[32:35], v[236:243], v[176:183], v[32:35], v209, v210 op_sel_hi:[0,0,0]
	v_mfma_scale_f32_16x16x128_f8f6f4 v[28:31], v[228:235], v[212:219], v[28:31], v209, v210 op_sel_hi:[0,0,0]
	v_mfma_scale_f32_16x16x128_f8f6f4 v[24:27], v[236:243], v[212:219], v[24:27], v209, v210 op_sel_hi:[0,0,0]
	v_mfma_scale_f32_16x16x128_f8f6f4 v[20:23], v[228:235], v[220:227], v[20:23], v209, v210 op_sel_hi:[0,0,0]
	v_mfma_scale_f32_16x16x128_f8f6f4 v[16:19], v[236:243], v[220:227], v[16:19], v209, v210 op_sel_hi:[0,0,0]
	s_setprio 0
	s_add_i32 s62, s62, 2
	s_add_u32 s34, s34, 0x100
	s_addc_u32 s35, s35, 0
	s_add_u32 s60, s60, 0x100
	s_addc_u32 s61, s61, 0
	s_cmp_gt_u32 s62, 13
	s_barrier
	s_cbranch_scc0 .LBB0_1112
	v_lshl_or_b32 v168, s31, 8, v207
	v_lshl_add_u32 v184, s30, 8, v190
	v_ashrrev_i32_e32 v169, 31, v168
	v_lshlrev_b64 v[0:1], 2, v[168:169]
	v_ashrrev_i32_e32 v185, 31, v184
	v_or_b32_e32 v230, 16, v184
	s_ashr_i32 s21, s30, 3
	v_lshl_add_u64 v[188:189], s[0:1], 0, v[0:1]
	v_lshlrev_b64 v[2:3], 13, v[184:185]
	v_ashrrev_i32_e32 v231, 31, v230
	s_mul_hi_i32 s23, s21, 0xc000
	s_mul_i32 s21, s21, 0xc000
	s_nop 15
	s_nop 15
	v_lshl_add_u64 v[172:173], v[188:189], 0, v[2:3]
	v_lshl_add_u64 v[174:175], v[184:185], 3, s[14:15]
	v_lshlrev_b64 v[2:3], 13, v[230:231]
	v_lshl_add_u64 v[182:183], v[230:231], 3, s[14:15]
	s_add_u32 s21, s10, s21
	global_load_dwordx2 v[228:229], v[174:175], off
	global_load_dwordx4 v[212:215], v[172:173], off
	global_load_dwordx4 v[216:219], v[172:173], off offset:16
	v_lshl_add_u64 v[176:177], v[188:189], 0, v[2:3]
	global_load_dwordx2 v[232:233], v[182:183], off
	global_load_dwordx4 v[220:223], v[176:177], off
	global_load_dwordx4 v[224:227], v[176:177], off offset:16
	s_addc_u32 s23, s11, s23
	v_lshl_add_u64 v[180:181], s[6:7], 0, v[0:1]
	s_add_u32 s30, s21, 0x904000
	v_lshl_add_u64 v[178:179], s[4:5], 0, v[0:1]
	global_load_dwordx4 v[12:15], v[180:181], off
	global_load_dwordx4 v[144:147], v[178:179], off
	global_load_dwordx4 v[8:11], v[178:179], off offset:16
	global_load_dwordx4 v[148:151], v[180:181], off offset:16
	s_addc_u32 s31, s23, 0
	v_lshl_add_u64 v[0:1], s[30:31], 0, v[0:1]
	global_load_dwordx4 v[4:7], v[0:1], off
	s_nop 0
	global_load_dwordx4 v[0:3], v[0:1], off offset:16
	v_mov_b32_e32 v249, 0
	v_mov_b32_e32 v248, 0x40000
	v_lshl_add_u64 v[246:247], v[172:173], 0, v[248:249]
	global_load_dword v250, v[246:247], off
	global_load_dword v250, v[246:247], off offset:512
	global_load_dword v250, v[174:175], off offset:256
	v_mov_b32_e32 v248, 0x60000
	v_lshl_add_u64 v[246:247], v[172:173], 0, v[248:249]
	global_load_dword v250, v[246:247], off
	global_load_dword v250, v[246:247], off offset:512
	global_load_dword v250, v[174:175], off offset:384
	v_mov_b32_e32 v248, 0x100000
	v_lshl_add_u64 v[246:247], v[172:173], 0, v[248:249]
	global_load_dword v250, v[246:247], off
	global_load_dword v250, v[246:247], off offset:512
	global_load_dword v250, v[174:175], off offset:1024
	v_mov_b32_e32 v248, 0x120000
	v_lshl_add_u64 v[246:247], v[172:173], 0, v[248:249]
	global_load_dword v250, v[246:247], off
	global_load_dword v250, v[246:247], off offset:512
	global_load_dword v250, v[174:175], off offset:1152
	v_mov_b32_e32 v248, 0x140000
	v_lshl_add_u64 v[246:247], v[172:173], 0, v[248:249]
	global_load_dword v250, v[246:247], off
	global_load_dword v250, v[246:247], off offset:512
	global_load_dword v250, v[174:175], off offset:1280
	v_mov_b32_e32 v248, 0x160000
	v_lshl_add_u64 v[246:247], v[172:173], 0, v[248:249]
	global_load_dword v250, v[246:247], off
	global_load_dword v250, v[246:247], off offset:512
	global_load_dword v250, v[174:175], off offset:1408
	global_load_dword v250, v[172:173], off offset:512
	global_load_dword v250, v[176:177], off offset:512
	v_lshlrev_b64 v[170:171], 12, v[184:185]
	v_lshlrev_b64 v[186:187], 1, v[168:169]
	v_lshl_add_u64 v[170:171], s[12:13], 0, v[170:171]
	v_lshl_add_u64 v[170:171], v[170:171], 0, v[186:187]
	s_and_b64 vcc, exec, s[24:25]
	s_mov_b64 s[36:37], s[28:29]
	s_mov_b64 s[34:35], s[26:27]
	s_waitcnt vmcnt(0)
	v_sub_f32_e32 v215, v215, v228
	v_sub_f32_e32 v214, v214, v228
	v_sub_f32_e32 v213, v213, v228
	v_sub_f32_e32 v212, v212, v228
	v_sub_f32_e32 v219, v219, v228
	v_sub_f32_e32 v218, v218, v228
	v_sub_f32_e32 v217, v217, v228
	v_sub_f32_e32 v216, v216, v228
	v_sub_f32_e32 v223, v223, v232
	v_sub_f32_e32 v222, v222, v232
	v_sub_f32_e32 v221, v221, v232
	v_sub_f32_e32 v220, v220, v232
	v_sub_f32_e32 v225, v225, v232
	v_sub_f32_e32 v224, v224, v232
	v_sub_f32_e32 v227, v227, v232
	v_sub_f32_e32 v226, v226, v232
	v_pk_mul_f32 v[212:213], v[228:229], v[212:213] op_sel:[1,0]
	v_pk_mul_f32 v[214:215], v[228:229], v[214:215] op_sel:[1,0]
	v_pk_mul_f32 v[216:217], v[228:229], v[216:217] op_sel:[1,0]
	v_pk_mul_f32 v[218:219], v[228:229], v[218:219] op_sel:[1,0]
	v_pk_mul_f32 v[220:221], v[232:233], v[220:221] op_sel:[1,0]
	v_pk_mul_f32 v[222:223], v[232:233], v[222:223] op_sel:[1,0]
	v_pk_mul_f32 v[224:225], v[232:233], v[224:225] op_sel:[1,0]
	v_pk_mul_f32 v[226:227], v[232:233], v[226:227] op_sel:[1,0]
	v_pk_fma_f32 v[214:215], v[146:147], v[214:215], v[14:15]
	v_pk_fma_f32 v[212:213], v[144:145], v[212:213], v[12:13]
	v_pk_fma_f32 v[218:219], v[10:11], v[218:219], v[150:151]
	v_pk_fma_f32 v[216:217], v[8:9], v[216:217], v[148:149]
	v_pk_fma_f32 v[222:223], v[146:147], v[222:223], v[14:15]
	v_pk_fma_f32 v[220:221], v[144:145], v[220:221], v[12:13]
	v_pk_fma_f32 v[224:225], v[8:9], v[224:225], v[148:149]
	v_pk_fma_f32 v[226:227], v[10:11], v[226:227], v[150:151]
	v_pk_mul_f32 v[212:213], v[212:213], s[18:19] op_sel_hi:[1,0]
	v_pk_mul_f32 v[214:215], v[214:215], s[18:19] op_sel_hi:[1,0]
	v_pk_mul_f32 v[216:217], v[216:217], s[18:19] op_sel_hi:[1,0]
	v_pk_mul_f32 v[218:219], v[218:219], s[18:19] op_sel_hi:[1,0]
	v_pk_mul_f32 v[220:221], v[220:221], s[18:19] op_sel_hi:[1,0]
	v_pk_mul_f32 v[222:223], v[222:223], s[18:19] op_sel_hi:[1,0]
	v_pk_mul_f32 v[224:225], v[224:225], s[18:19] op_sel_hi:[1,0]
	v_pk_mul_f32 v[226:227], v[226:227], s[18:19] op_sel_hi:[1,0]
	v_pk_fma_f32 v[142:143], v[142:143], v[6:7], v[214:215]
	v_pk_fma_f32 v[140:141], v[140:141], v[4:5], v[212:213]
	v_pk_fma_f32 v[138:139], v[138:139], v[2:3], v[218:219]
	v_pk_fma_f32 v[136:137], v[136:137], v[0:1], v[216:217]
	v_pk_fma_f32 v[212:213], v[134:135], v[6:7], v[222:223]
	v_pk_fma_f32 v[214:215], v[132:133], v[4:5], v[220:221]
	v_cvt_pk_bf16_f32 v132, v140, v141
	v_cvt_pk_bf16_f32 v133, v142, v143
	v_cvt_pk_bf16_f32 v134, v136, v137
	v_cvt_pk_bf16_f32 v135, v138, v139
	v_pk_fma_f32 v[128:129], v[128:129], v[0:1], v[224:225]
	global_store_dwordx4 v[170:171], v[132:135], off
	v_or_b32_e32 v136, 32, v184
	v_ashrrev_i32_e32 v137, 31, v136
	v_pk_fma_f32 v[134:135], v[130:131], v[2:3], v[226:227]
	v_cvt_pk_bf16_f32 v130, v214, v215
	v_cvt_pk_bf16_f32 v131, v212, v213
	v_cvt_pk_bf16_f32 v132, v128, v129
	v_lshlrev_b64 v[128:129], 12, v[230:231]
	v_lshl_add_u64 v[128:129], s[12:13], 0, v[128:129]
	v_lshl_add_u64 v[128:129], v[128:129], 0, v[186:187]
	v_or_b32_e32 v226, 48, v184
	v_cvt_pk_bf16_f32 v133, v134, v135
	global_store_dwordx4 v[128:129], v[130:133], off
	v_ashrrev_i32_e32 v227, 31, v226
	v_lshlrev_b64 v[134:135], 13, v[226:227]
	v_lshlrev_b64 v[130:131], 13, v[136:137]
	v_lshl_add_u64 v[132:133], v[136:137], 3, s[14:15]
	v_lshl_add_u64 v[138:139], v[226:227], 3, s[14:15]
	v_lshl_add_u64 v[130:131], v[188:189], 0, v[130:131]
	global_load_dwordx2 v[224:225], v[132:133], off
	global_load_dwordx4 v[140:143], v[130:131], off
	global_load_dwordx4 v[212:215], v[130:131], off offset:16
	v_lshl_add_u64 v[134:135], v[188:189], 0, v[134:135]
	global_load_dwordx2 v[228:229], v[138:139], off
	global_load_dwordx4 v[216:219], v[134:135], off
	global_load_dwordx4 v[220:223], v[134:135], off offset:16
	v_lshlrev_b64 v[136:137], 12, v[136:137]
	v_lshl_add_u64 v[136:137], s[12:13], 0, v[136:137]
	v_lshlrev_b64 v[226:227], 12, v[226:227]
	v_lshl_add_u64 v[136:137], v[136:137], 0, v[186:187]
	v_add_u32_e32 v230, 0x80, v184
	v_ashrrev_i32_e32 v231, 31, v230
	v_add_u32_e32 v232, 0xa0, v184
	v_ashrrev_i32_e32 v233, 31, v232
	s_waitcnt vmcnt(0)
	v_sub_f32_e32 v143, v143, v224
	v_sub_f32_e32 v142, v142, v224
	v_sub_f32_e32 v141, v141, v224
	v_sub_f32_e32 v140, v140, v224
	v_sub_f32_e32 v217, v217, v228
	v_sub_f32_e32 v216, v216, v228
	v_sub_f32_e32 v221, v221, v228
	v_sub_f32_e32 v220, v220, v228
	v_sub_f32_e32 v215, v215, v224
	v_sub_f32_e32 v214, v214, v224
	v_sub_f32_e32 v213, v213, v224
	v_sub_f32_e32 v212, v212, v224
	v_sub_f32_e32 v223, v223, v228
	v_sub_f32_e32 v222, v222, v228
	v_pk_mul_f32 v[140:141], v[224:225], v[140:141] op_sel:[1,0]
	v_pk_mul_f32 v[142:143], v[224:225], v[142:143] op_sel:[1,0]
	v_pk_mul_f32 v[216:217], v[228:229], v[216:217] op_sel:[1,0]
	v_pk_mul_f32 v[220:221], v[228:229], v[220:221] op_sel:[1,0]
	v_sub_f32_e32 v219, v219, v228
	v_sub_f32_e32 v218, v218, v228
	v_pk_mul_f32 v[212:213], v[224:225], v[212:213] op_sel:[1,0]
	v_pk_mul_f32 v[214:215], v[224:225], v[214:215] op_sel:[1,0]
	v_pk_mul_f32 v[222:223], v[228:229], v[222:223] op_sel:[1,0]
	v_pk_fma_f32 v[142:143], v[146:147], v[142:143], v[14:15]
	v_pk_fma_f32 v[140:141], v[144:145], v[140:141], v[12:13]
	v_pk_fma_f32 v[216:217], v[144:145], v[216:217], v[12:13]
	v_pk_fma_f32 v[220:221], v[8:9], v[220:221], v[148:149]
	v_pk_mul_f32 v[218:219], v[228:229], v[218:219] op_sel:[1,0]
	v_pk_fma_f32 v[214:215], v[10:11], v[214:215], v[150:151]
	v_pk_fma_f32 v[212:213], v[8:9], v[212:213], v[148:149]
	v_pk_fma_f32 v[222:223], v[10:11], v[222:223], v[150:151]
	v_pk_mul_f32 v[140:141], v[140:141], s[18:19] op_sel_hi:[1,0]
	v_pk_mul_f32 v[142:143], v[142:143], s[18:19] op_sel_hi:[1,0]
	v_pk_mul_f32 v[216:217], v[216:217], s[18:19] op_sel_hi:[1,0]
	v_pk_mul_f32 v[220:221], v[220:221], s[18:19] op_sel_hi:[1,0]
	v_pk_fma_f32 v[218:219], v[146:147], v[218:219], v[14:15]
	v_pk_mul_f32 v[212:213], v[212:213], s[18:19] op_sel_hi:[1,0]
	v_pk_mul_f32 v[214:215], v[214:215], s[18:19] op_sel_hi:[1,0]
	v_pk_mul_f32 v[222:223], v[222:223], s[18:19] op_sel_hi:[1,0]
	v_pk_fma_f32 v[126:127], v[126:127], v[6:7], v[142:143]
	v_pk_fma_f32 v[124:125], v[124:125], v[4:5], v[140:141]
	v_pk_fma_f32 v[116:117], v[116:117], v[4:5], v[216:217]
	v_pk_fma_f32 v[142:143], v[112:113], v[0:1], v[220:221]
	v_cvt_pk_bf16_f32 v112, v124, v125
	v_pk_mul_f32 v[218:219], v[218:219], s[18:19] op_sel_hi:[1,0]
	v_pk_fma_f32 v[122:123], v[122:123], v[2:3], v[214:215]
	v_pk_fma_f32 v[120:121], v[120:121], v[0:1], v[212:213]
	v_pk_fma_f32 v[140:141], v[114:115], v[2:3], v[222:223]
	v_cvt_pk_bf16_f32 v113, v126, v127
	v_cvt_pk_bf16_f32 v114, v120, v121
	v_cvt_pk_bf16_f32 v115, v122, v123
	global_store_dwordx4 v[136:137], v[112:115], off
	v_pk_fma_f32 v[118:119], v[118:119], v[6:7], v[218:219]
	v_lshl_add_u64 v[122:123], v[230:231], 3, s[14:15]
	v_cvt_pk_bf16_f32 v112, v116, v117
	v_lshl_add_u64 v[116:117], s[12:13], 0, v[226:227]
	v_cvt_pk_bf16_f32 v113, v118, v119
	v_lshl_add_u64 v[116:117], v[116:117], 0, v[186:187]
	v_cvt_pk_bf16_f32 v114, v142, v143
	v_cvt_pk_bf16_f32 v115, v140, v141
	global_store_dwordx4 v[116:117], v[112:115], off
	v_lshlrev_b64 v[140:141], 13, v[232:233]
	s_nop 0
	v_lshlrev_b64 v[112:113], 13, v[230:231]
	v_lshl_add_u64 v[118:119], v[188:189], 0, v[112:113]
	v_add_u32_e32 v112, 0x90, v184
	v_ashrrev_i32_e32 v113, 31, v112
	v_lshlrev_b64 v[114:115], 13, v[112:113]
	v_lshl_add_u64 v[126:127], v[112:113], 3, s[14:15]
	global_load_dwordx2 v[142:143], v[122:123], off
	global_load_dwordx4 v[212:215], v[118:119], off
	global_load_dwordx4 v[216:219], v[118:119], off offset:16
	v_lshl_add_u64 v[124:125], v[188:189], 0, v[114:115]
	global_load_dwordx2 v[228:229], v[126:127], off
	global_load_dwordx4 v[220:223], v[124:125], off
	global_load_dwordx4 v[224:227], v[124:125], off offset:16
	v_lshlrev_b64 v[114:115], 12, v[230:231]
	v_lshlrev_b64 v[120:121], 12, v[112:113]
	v_lshl_add_u64 v[230:231], s[12:13], 0, v[114:115]
	v_lshl_add_u64 v[120:121], s[12:13], 0, v[120:121]
	v_lshl_add_u64 v[114:115], v[188:189], 0, v[140:141]
	v_lshl_add_u64 v[140:141], v[230:231], 0, v[186:187]
	v_lshl_add_u64 v[120:121], v[120:121], 0, v[186:187]
	v_lshl_add_u64 v[112:113], v[232:233], 3, s[14:15]
	s_waitcnt vmcnt(0)
	v_sub_f32_e32 v215, v215, v142
	v_sub_f32_e32 v214, v214, v142
	v_sub_f32_e32 v213, v213, v142
	v_sub_f32_e32 v212, v212, v142
	v_sub_f32_e32 v219, v219, v142
	v_sub_f32_e32 v218, v218, v142
	v_sub_f32_e32 v217, v217, v142
	v_sub_f32_e32 v216, v216, v142
	v_sub_f32_e32 v223, v223, v228
	v_sub_f32_e32 v222, v222, v228
	v_sub_f32_e32 v221, v221, v228
	v_sub_f32_e32 v220, v220, v228
	v_sub_f32_e32 v225, v225, v228
	v_sub_f32_e32 v224, v224, v228
	v_sub_f32_e32 v227, v227, v228
	v_sub_f32_e32 v226, v226, v228
	v_pk_mul_f32 v[212:213], v[142:143], v[212:213] op_sel:[1,0]
	v_pk_mul_f32 v[214:215], v[142:143], v[214:215] op_sel:[1,0]
	v_pk_mul_f32 v[216:217], v[142:143], v[216:217] op_sel:[1,0]
	v_pk_mul_f32 v[142:143], v[142:143], v[218:219] op_sel:[1,0]
	v_pk_mul_f32 v[218:219], v[228:229], v[220:221] op_sel:[1,0]
	v_pk_mul_f32 v[220:221], v[228:229], v[222:223] op_sel:[1,0]
	v_pk_mul_f32 v[222:223], v[228:229], v[224:225] op_sel:[1,0]
	v_pk_mul_f32 v[224:225], v[228:229], v[226:227] op_sel:[1,0]
	v_pk_fma_f32 v[212:213], v[144:145], v[212:213], v[12:13]
	v_pk_fma_f32 v[222:223], v[8:9], v[222:223], v[148:149]
	v_pk_fma_f32 v[214:215], v[146:147], v[214:215], v[14:15]
	v_pk_fma_f32 v[142:143], v[10:11], v[142:143], v[150:151]
	v_pk_fma_f32 v[216:217], v[8:9], v[216:217], v[148:149]
	v_pk_fma_f32 v[218:219], v[144:145], v[218:219], v[12:13]
	v_pk_fma_f32 v[224:225], v[10:11], v[224:225], v[150:151]
	v_pk_mul_f32 v[212:213], v[212:213], s[18:19] op_sel_hi:[1,0]
	v_pk_mul_f32 v[222:223], v[222:223], s[18:19] op_sel_hi:[1,0]
	v_pk_fma_f32 v[220:221], v[146:147], v[220:221], v[14:15]
	v_pk_mul_f32 v[214:215], v[214:215], s[18:19] op_sel_hi:[1,0]
	v_pk_mul_f32 v[216:217], v[216:217], s[18:19] op_sel_hi:[1,0]
	v_pk_mul_f32 v[142:143], v[142:143], s[18:19] op_sel_hi:[1,0]
	v_pk_mul_f32 v[218:219], v[218:219], s[18:19] op_sel_hi:[1,0]
	v_pk_mul_f32 v[224:225], v[224:225], s[18:19] op_sel_hi:[1,0]
	v_pk_fma_f32 v[108:109], v[108:109], v[4:5], v[212:213]
	v_pk_fma_f32 v[212:213], v[96:97], v[0:1], v[222:223]
	v_cvt_pk_bf16_f32 v96, v108, v109
	v_pk_mul_f32 v[220:221], v[220:221], s[18:19] op_sel_hi:[1,0]
	v_pk_fma_f32 v[110:111], v[110:111], v[6:7], v[214:215]
	v_pk_fma_f32 v[106:107], v[106:107], v[2:3], v[142:143]
	v_pk_fma_f32 v[104:105], v[104:105], v[0:1], v[216:217]
	v_pk_fma_f32 v[100:101], v[100:101], v[4:5], v[218:219]
	v_pk_fma_f32 v[142:143], v[98:99], v[2:3], v[224:225]
	v_cvt_pk_bf16_f32 v97, v110, v111
	v_cvt_pk_bf16_f32 v98, v104, v105
	v_cvt_pk_bf16_f32 v99, v106, v107
	global_store_dwordx4 v[140:141], v[96:99], off
	v_pk_fma_f32 v[102:103], v[102:103], v[6:7], v[220:221]
	s_nop 0
	v_cvt_pk_bf16_f32 v96, v100, v101
	v_cvt_pk_bf16_f32 v97, v102, v103
	v_cvt_pk_bf16_f32 v98, v212, v213
	v_cvt_pk_bf16_f32 v99, v142, v143
	global_store_dwordx4 v[120:121], v[96:99], off
	global_load_dwordx2 v[142:143], v[112:113], off
	global_load_dwordx4 v[104:107], v[114:115], off
	global_load_dwordx4 v[108:111], v[114:115], off offset:16
	v_add_u32_e32 v96, 0xb0, v184
	v_ashrrev_i32_e32 v97, 31, v96
	v_lshlrev_b64 v[98:99], 13, v[96:97]
	v_lshl_add_u64 v[102:103], v[96:97], 3, s[14:15]
	v_lshl_add_u64 v[100:101], v[188:189], 0, v[98:99]
	global_load_dwordx2 v[184:185], v[102:103], off
	global_load_dwordx4 v[212:215], v[100:101], off
	global_load_dwordx4 v[216:219], v[100:101], off offset:16
	v_lshlrev_b64 v[98:99], 12, v[232:233]
	v_lshlrev_b64 v[96:97], 12, v[96:97]
	v_lshl_add_u64 v[98:99], s[12:13], 0, v[98:99]
	v_lshl_add_u64 v[96:97], s[12:13], 0, v[96:97]
	v_lshl_add_u64 v[98:99], v[98:99], 0, v[186:187]
	v_lshl_add_u64 v[96:97], v[96:97], 0, v[186:187]
	s_waitcnt vmcnt(0)
	v_sub_f32_e32 v107, v107, v142
	v_sub_f32_e32 v106, v106, v142
	v_sub_f32_e32 v105, v105, v142
	v_sub_f32_e32 v104, v104, v142
	v_sub_f32_e32 v111, v111, v142
	v_sub_f32_e32 v110, v110, v142
	v_sub_f32_e32 v109, v109, v142
	v_sub_f32_e32 v108, v108, v142
	v_sub_f32_e32 v187, v215, v184
	v_sub_f32_e32 v186, v214, v184
	v_sub_f32_e32 v189, v213, v184
	v_sub_f32_e32 v188, v212, v184
	v_sub_f32_e32 v213, v219, v184
	v_sub_f32_e32 v212, v218, v184
	v_sub_f32_e32 v215, v217, v184
	v_sub_f32_e32 v214, v216, v184
	v_pk_mul_f32 v[104:105], v[142:143], v[104:105] op_sel:[1,0]
	v_pk_mul_f32 v[106:107], v[142:143], v[106:107] op_sel:[1,0]
	v_pk_mul_f32 v[108:109], v[142:143], v[108:109] op_sel:[1,0]
	v_pk_mul_f32 v[110:111], v[142:143], v[110:111] op_sel:[1,0]
	v_pk_mul_f32 v[142:143], v[184:185], v[188:189] op_sel:[1,0]
	v_pk_mul_f32 v[186:187], v[184:185], v[186:187] op_sel:[1,0]
	v_pk_mul_f32 v[188:189], v[184:185], v[214:215] op_sel:[1,0]
	v_pk_mul_f32 v[184:185], v[184:185], v[212:213] op_sel:[1,0]
	v_pk_fma_f32 v[106:107], v[146:147], v[106:107], v[14:15]
	v_pk_fma_f32 v[104:105], v[144:145], v[104:105], v[12:13]
	v_pk_fma_f32 v[110:111], v[10:11], v[110:111], v[150:151]
	v_pk_fma_f32 v[108:109], v[8:9], v[108:109], v[148:149]
	v_pk_fma_f32 v[10:11], v[10:11], v[184:185], v[150:151]
	v_pk_fma_f32 v[8:9], v[8:9], v[188:189], v[148:149]
	v_pk_fma_f32 v[14:15], v[146:147], v[186:187], v[14:15]
	v_pk_fma_f32 v[12:13], v[144:145], v[142:143], v[12:13]
	v_pk_mul_f32 v[104:105], v[104:105], s[18:19] op_sel_hi:[1,0]
	v_pk_mul_f32 v[106:107], v[106:107], s[18:19] op_sel_hi:[1,0]
	v_pk_mul_f32 v[108:109], v[108:109], s[18:19] op_sel_hi:[1,0]
	v_pk_mul_f32 v[110:111], v[110:111], s[18:19] op_sel_hi:[1,0]
	v_pk_mul_f32 v[8:9], v[8:9], s[18:19] op_sel_hi:[1,0]
	v_pk_mul_f32 v[10:11], v[10:11], s[18:19] op_sel_hi:[1,0]
	v_pk_mul_f32 v[12:13], v[12:13], s[18:19] op_sel_hi:[1,0]
	v_pk_mul_f32 v[14:15], v[14:15], s[18:19] op_sel_hi:[1,0]
	v_pk_fma_f32 v[94:95], v[94:95], v[6:7], v[106:107]
	v_pk_fma_f32 v[92:93], v[92:93], v[4:5], v[104:105]
	v_pk_fma_f32 v[90:91], v[90:91], v[2:3], v[110:111]
	v_pk_fma_f32 v[88:89], v[88:89], v[0:1], v[108:109]
	v_pk_fma_f32 v[10:11], v[82:83], v[2:3], v[10:11]
	v_pk_fma_f32 v[8:9], v[80:81], v[0:1], v[8:9]
	v_cvt_pk_bf16_f32 v0, v92, v93
	v_cvt_pk_bf16_f32 v1, v94, v95
	v_cvt_pk_bf16_f32 v2, v88, v89
	v_cvt_pk_bf16_f32 v3, v90, v91
	v_pk_fma_f32 v[6:7], v[86:87], v[6:7], v[14:15]
	v_pk_fma_f32 v[4:5], v[84:85], v[4:5], v[12:13]
	global_store_dwordx4 v[98:99], v[0:3], off
	s_nop 1
	v_cvt_pk_bf16_f32 v0, v4, v5
	v_cvt_pk_bf16_f32 v1, v6, v7
	v_cvt_pk_bf16_f32 v2, v8, v9
	v_cvt_pk_bf16_f32 v3, v10, v11
	global_store_dwordx4 v[96:97], v[0:3], off
	global_load_dwordx2 v[142:143], v[174:175], off
	global_load_dwordx4 v[88:91], v[172:173], off offset:512
	global_load_dwordx4 v[92:95], v[172:173], off offset:528
	global_load_dwordx2 v[144:145], v[182:183], off
	global_load_dwordx4 v[104:107], v[176:177], off offset:512
	global_load_dwordx4 v[108:111], v[176:177], off offset:528
	global_load_dwordx4 v[12:15], v[180:181], off offset:512
	global_load_dwordx4 v[80:83], v[178:179], off offset:512
	global_load_dwordx4 v[8:11], v[178:179], off offset:528
	global_load_dwordx4 v[84:87], v[180:181], off offset:528
	v_or_b32_e32 v0, 0x80, v168
	v_ashrrev_i32_e32 v1, 31, v0
	v_lshl_add_u64 v[0:1], v[0:1], 2, s[30:31]
	global_load_dwordx4 v[4:7], v[0:1], off
	s_nop 0
	global_load_dwordx4 v[0:3], v[0:1], off offset:16
	s_mov_b32 s31, s22
	s_mov_b32 s30, s20
	s_waitcnt vmcnt(0)
	v_sub_f32_e32 v91, v91, v142
	v_sub_f32_e32 v90, v90, v142
	v_sub_f32_e32 v89, v89, v142
	v_sub_f32_e32 v88, v88, v142
	v_sub_f32_e32 v95, v95, v142
	v_sub_f32_e32 v94, v94, v142
	v_sub_f32_e32 v93, v93, v142
	v_sub_f32_e32 v92, v92, v142
	v_sub_f32_e32 v111, v111, v144
	v_sub_f32_e32 v110, v110, v144
	v_sub_f32_e32 v109, v109, v144
	v_sub_f32_e32 v108, v108, v144
	v_sub_f32_e32 v107, v107, v144
	v_sub_f32_e32 v106, v106, v144
	v_sub_f32_e32 v105, v105, v144
	v_sub_f32_e32 v104, v104, v144
	v_pk_mul_f32 v[88:89], v[142:143], v[88:89] op_sel:[1,0]
	v_pk_mul_f32 v[90:91], v[142:143], v[90:91] op_sel:[1,0]
	v_pk_mul_f32 v[92:93], v[142:143], v[92:93] op_sel:[1,0]
	v_pk_mul_f32 v[94:95], v[142:143], v[94:95] op_sel:[1,0]
	v_pk_mul_f32 v[108:109], v[144:145], v[108:109] op_sel:[1,0]
	v_pk_mul_f32 v[110:111], v[144:145], v[110:111] op_sel:[1,0]
	v_pk_mul_f32 v[104:105], v[144:145], v[104:105] op_sel:[1,0]
	v_pk_mul_f32 v[106:107], v[144:145], v[106:107] op_sel:[1,0]
	v_pk_fma_f32 v[90:91], v[82:83], v[90:91], v[14:15]
	v_pk_fma_f32 v[88:89], v[80:81], v[88:89], v[12:13]
	v_pk_fma_f32 v[94:95], v[10:11], v[94:95], v[86:87]
	v_pk_fma_f32 v[92:93], v[8:9], v[92:93], v[84:85]
	v_pk_fma_f32 v[110:111], v[10:11], v[110:111], v[86:87]
	v_pk_fma_f32 v[108:109], v[8:9], v[108:109], v[84:85]
	v_pk_fma_f32 v[106:107], v[82:83], v[106:107], v[14:15]
	v_pk_fma_f32 v[104:105], v[80:81], v[104:105], v[12:13]
	v_pk_mul_f32 v[88:89], v[88:89], s[18:19] op_sel_hi:[1,0]
	v_pk_mul_f32 v[90:91], v[90:91], s[18:19] op_sel_hi:[1,0]
	v_pk_mul_f32 v[92:93], v[92:93], s[18:19] op_sel_hi:[1,0]
	v_pk_mul_f32 v[94:95], v[94:95], s[18:19] op_sel_hi:[1,0]
	v_pk_mul_f32 v[108:109], v[108:109], s[18:19] op_sel_hi:[1,0]
	v_pk_mul_f32 v[110:111], v[110:111], s[18:19] op_sel_hi:[1,0]
	v_pk_mul_f32 v[104:105], v[104:105], s[18:19] op_sel_hi:[1,0]
	v_pk_mul_f32 v[106:107], v[106:107], s[18:19] op_sel_hi:[1,0]
	v_pk_fma_f32 v[78:79], v[78:79], v[6:7], v[90:91]
	v_pk_fma_f32 v[76:77], v[76:77], v[4:5], v[88:89]
	v_pk_fma_f32 v[74:75], v[74:75], v[2:3], v[94:95]
	v_pk_fma_f32 v[72:73], v[72:73], v[0:1], v[92:93]
	v_pk_fma_f32 v[88:89], v[66:67], v[2:3], v[110:111]
	v_pk_fma_f32 v[90:91], v[64:65], v[0:1], v[108:109]
	v_cvt_pk_bf16_f32 v64, v76, v77
	v_cvt_pk_bf16_f32 v65, v78, v79
	v_cvt_pk_bf16_f32 v66, v72, v73
	v_cvt_pk_bf16_f32 v67, v74, v75
	v_pk_fma_f32 v[70:71], v[70:71], v[6:7], v[106:107]
	v_pk_fma_f32 v[68:69], v[68:69], v[4:5], v[104:105]
	global_store_dwordx4 v[170:171], v[64:67], off offset:256
	s_nop 1
	v_cvt_pk_bf16_f32 v64, v68, v69
	v_cvt_pk_bf16_f32 v65, v70, v71
	v_cvt_pk_bf16_f32 v66, v90, v91
	v_cvt_pk_bf16_f32 v67, v88, v89
	global_store_dwordx4 v[128:129], v[64:67], off offset:256
	global_load_dwordx2 v[88:89], v[132:133], off
	global_load_dwordx4 v[64:67], v[130:131], off offset:512
	global_load_dwordx4 v[68:71], v[130:131], off offset:528
	global_load_dwordx2 v[90:91], v[138:139], off
	global_load_dwordx4 v[72:75], v[134:135], off offset:512
	global_load_dwordx4 v[76:79], v[134:135], off offset:528
	s_waitcnt vmcnt(0)
	v_sub_f32_e32 v67, v67, v88
	v_sub_f32_e32 v66, v66, v88
	v_sub_f32_e32 v65, v65, v88
	v_sub_f32_e32 v64, v64, v88
	v_sub_f32_e32 v71, v71, v88
	v_sub_f32_e32 v70, v70, v88
	v_sub_f32_e32 v69, v69, v88
	v_sub_f32_e32 v68, v68, v88
	v_sub_f32_e32 v79, v79, v90
	v_sub_f32_e32 v78, v78, v90
	v_sub_f32_e32 v77, v77, v90
	v_sub_f32_e32 v76, v76, v90
	v_sub_f32_e32 v75, v75, v90
	v_sub_f32_e32 v74, v74, v90
	v_sub_f32_e32 v73, v73, v90
	v_sub_f32_e32 v72, v72, v90
	v_pk_mul_f32 v[64:65], v[88:89], v[64:65] op_sel:[1,0]
	v_pk_mul_f32 v[66:67], v[88:89], v[66:67] op_sel:[1,0]
	v_pk_mul_f32 v[68:69], v[88:89], v[68:69] op_sel:[1,0]
	v_pk_mul_f32 v[70:71], v[88:89], v[70:71] op_sel:[1,0]
	v_pk_mul_f32 v[76:77], v[90:91], v[76:77] op_sel:[1,0]
	v_pk_mul_f32 v[78:79], v[90:91], v[78:79] op_sel:[1,0]
	v_pk_mul_f32 v[72:73], v[90:91], v[72:73] op_sel:[1,0]
	v_pk_mul_f32 v[74:75], v[90:91], v[74:75] op_sel:[1,0]
	v_pk_fma_f32 v[66:67], v[82:83], v[66:67], v[14:15]
	v_pk_fma_f32 v[64:65], v[80:81], v[64:65], v[12:13]
	v_pk_fma_f32 v[70:71], v[10:11], v[70:71], v[86:87]
	v_pk_fma_f32 v[68:69], v[8:9], v[68:69], v[84:85]
	v_pk_fma_f32 v[78:79], v[10:11], v[78:79], v[86:87]
	v_pk_fma_f32 v[76:77], v[8:9], v[76:77], v[84:85]
	v_pk_fma_f32 v[74:75], v[82:83], v[74:75], v[14:15]
	v_pk_fma_f32 v[72:73], v[80:81], v[72:73], v[12:13]
	v_pk_mul_f32 v[64:65], v[64:65], s[18:19] op_sel_hi:[1,0]
	v_pk_mul_f32 v[66:67], v[66:67], s[18:19] op_sel_hi:[1,0]
	v_pk_mul_f32 v[68:69], v[68:69], s[18:19] op_sel_hi:[1,0]
	v_pk_mul_f32 v[70:71], v[70:71], s[18:19] op_sel_hi:[1,0]
	v_pk_mul_f32 v[76:77], v[76:77], s[18:19] op_sel_hi:[1,0]
	v_pk_mul_f32 v[78:79], v[78:79], s[18:19] op_sel_hi:[1,0]
	v_pk_mul_f32 v[72:73], v[72:73], s[18:19] op_sel_hi:[1,0]
	v_pk_mul_f32 v[74:75], v[74:75], s[18:19] op_sel_hi:[1,0]
	v_pk_fma_f32 v[62:63], v[62:63], v[6:7], v[66:67]
	v_pk_fma_f32 v[60:61], v[60:61], v[4:5], v[64:65]
	v_pk_fma_f32 v[58:59], v[58:59], v[2:3], v[70:71]
	v_pk_fma_f32 v[56:57], v[56:57], v[0:1], v[68:69]
	v_pk_fma_f32 v[64:65], v[50:51], v[2:3], v[78:79]
	v_pk_fma_f32 v[66:67], v[48:49], v[0:1], v[76:77]
	v_cvt_pk_bf16_f32 v48, v60, v61
	v_cvt_pk_bf16_f32 v49, v62, v63
	v_cvt_pk_bf16_f32 v50, v56, v57
	v_cvt_pk_bf16_f32 v51, v58, v59
	v_pk_fma_f32 v[54:55], v[54:55], v[6:7], v[74:75]
	v_pk_fma_f32 v[52:53], v[52:53], v[4:5], v[72:73]
	global_store_dwordx4 v[136:137], v[48:51], off offset:256
	s_nop 1
	v_cvt_pk_bf16_f32 v48, v52, v53
	v_cvt_pk_bf16_f32 v49, v54, v55
	v_cvt_pk_bf16_f32 v50, v66, v67
	v_cvt_pk_bf16_f32 v51, v64, v65
	global_store_dwordx4 v[116:117], v[48:51], off offset:256
	global_load_dwordx2 v[64:65], v[122:123], off
	global_load_dwordx4 v[48:51], v[118:119], off offset:512
	global_load_dwordx4 v[52:55], v[118:119], off offset:528
	global_load_dwordx2 v[66:67], v[126:127], off
	global_load_dwordx4 v[56:59], v[124:125], off offset:512
	global_load_dwordx4 v[60:63], v[124:125], off offset:528
	s_waitcnt vmcnt(0)
	v_sub_f32_e32 v51, v51, v64
	v_sub_f32_e32 v50, v50, v64
	v_sub_f32_e32 v49, v49, v64
	v_sub_f32_e32 v48, v48, v64
	v_sub_f32_e32 v55, v55, v64
	v_sub_f32_e32 v54, v54, v64
	v_sub_f32_e32 v53, v53, v64
	v_sub_f32_e32 v52, v52, v64
	v_sub_f32_e32 v63, v63, v66
	v_sub_f32_e32 v62, v62, v66
	v_sub_f32_e32 v61, v61, v66
	v_sub_f32_e32 v60, v60, v66
	v_sub_f32_e32 v59, v59, v66
	v_sub_f32_e32 v58, v58, v66
	v_sub_f32_e32 v57, v57, v66
	v_sub_f32_e32 v56, v56, v66
	v_pk_mul_f32 v[48:49], v[64:65], v[48:49] op_sel:[1,0]
	v_pk_mul_f32 v[50:51], v[64:65], v[50:51] op_sel:[1,0]
	v_pk_mul_f32 v[52:53], v[64:65], v[52:53] op_sel:[1,0]
	v_pk_mul_f32 v[54:55], v[64:65], v[54:55] op_sel:[1,0]
	v_pk_mul_f32 v[60:61], v[66:67], v[60:61] op_sel:[1,0]
	v_pk_mul_f32 v[62:63], v[66:67], v[62:63] op_sel:[1,0]
	v_pk_mul_f32 v[56:57], v[66:67], v[56:57] op_sel:[1,0]
	v_pk_mul_f32 v[58:59], v[66:67], v[58:59] op_sel:[1,0]
	v_pk_fma_f32 v[50:51], v[82:83], v[50:51], v[14:15]
	v_pk_fma_f32 v[48:49], v[80:81], v[48:49], v[12:13]
	v_pk_fma_f32 v[54:55], v[10:11], v[54:55], v[86:87]
	v_pk_fma_f32 v[52:53], v[8:9], v[52:53], v[84:85]
	v_pk_fma_f32 v[62:63], v[10:11], v[62:63], v[86:87]
	v_pk_fma_f32 v[60:61], v[8:9], v[60:61], v[84:85]
	v_pk_fma_f32 v[58:59], v[82:83], v[58:59], v[14:15]
	v_pk_fma_f32 v[56:57], v[80:81], v[56:57], v[12:13]
	v_pk_mul_f32 v[48:49], v[48:49], s[18:19] op_sel_hi:[1,0]
	v_pk_mul_f32 v[50:51], v[50:51], s[18:19] op_sel_hi:[1,0]
	v_pk_mul_f32 v[52:53], v[52:53], s[18:19] op_sel_hi:[1,0]
	v_pk_mul_f32 v[54:55], v[54:55], s[18:19] op_sel_hi:[1,0]
	v_pk_mul_f32 v[60:61], v[60:61], s[18:19] op_sel_hi:[1,0]
	v_pk_mul_f32 v[62:63], v[62:63], s[18:19] op_sel_hi:[1,0]
	v_pk_mul_f32 v[56:57], v[56:57], s[18:19] op_sel_hi:[1,0]
	v_pk_mul_f32 v[58:59], v[58:59], s[18:19] op_sel_hi:[1,0]
	v_pk_fma_f32 v[46:47], v[46:47], v[6:7], v[50:51]
	v_pk_fma_f32 v[44:45], v[44:45], v[4:5], v[48:49]
	v_pk_fma_f32 v[42:43], v[42:43], v[2:3], v[54:55]
	v_pk_fma_f32 v[40:41], v[40:41], v[0:1], v[52:53]
	v_pk_fma_f32 v[48:49], v[34:35], v[2:3], v[62:63]
	v_pk_fma_f32 v[50:51], v[32:33], v[0:1], v[60:61]
	v_cvt_pk_bf16_f32 v32, v44, v45
	v_cvt_pk_bf16_f32 v33, v46, v47
	v_cvt_pk_bf16_f32 v34, v40, v41
	v_cvt_pk_bf16_f32 v35, v42, v43
	v_pk_fma_f32 v[38:39], v[38:39], v[6:7], v[58:59]
	v_pk_fma_f32 v[36:37], v[36:37], v[4:5], v[56:57]
	global_store_dwordx4 v[140:141], v[32:35], off offset:256
	s_nop 1
	v_cvt_pk_bf16_f32 v32, v36, v37
	v_cvt_pk_bf16_f32 v33, v38, v39
	v_cvt_pk_bf16_f32 v34, v50, v51
	v_cvt_pk_bf16_f32 v35, v48, v49
	global_store_dwordx4 v[120:121], v[32:35], off offset:256
	global_load_dwordx2 v[48:49], v[112:113], off
	global_load_dwordx4 v[32:35], v[114:115], off offset:512
	global_load_dwordx4 v[36:39], v[114:115], off offset:528
	global_load_dwordx2 v[50:51], v[102:103], off
	global_load_dwordx4 v[40:43], v[100:101], off offset:512
	global_load_dwordx4 v[44:47], v[100:101], off offset:528
	s_waitcnt vmcnt(0)
	v_sub_f32_e32 v35, v35, v48
	v_sub_f32_e32 v34, v34, v48
	v_sub_f32_e32 v33, v33, v48
	v_sub_f32_e32 v32, v32, v48
	v_sub_f32_e32 v39, v39, v48
	v_sub_f32_e32 v38, v38, v48
	v_sub_f32_e32 v37, v37, v48
	v_sub_f32_e32 v36, v36, v48
	v_sub_f32_e32 v47, v47, v50
	v_sub_f32_e32 v46, v46, v50
	v_sub_f32_e32 v45, v45, v50
	v_sub_f32_e32 v44, v44, v50
	v_sub_f32_e32 v43, v43, v50
	v_sub_f32_e32 v42, v42, v50
	v_sub_f32_e32 v41, v41, v50
	v_sub_f32_e32 v40, v40, v50
	v_pk_mul_f32 v[32:33], v[48:49], v[32:33] op_sel:[1,0]
	v_pk_mul_f32 v[34:35], v[48:49], v[34:35] op_sel:[1,0]
	v_pk_mul_f32 v[36:37], v[48:49], v[36:37] op_sel:[1,0]
	v_pk_mul_f32 v[38:39], v[48:49], v[38:39] op_sel:[1,0]
	v_pk_mul_f32 v[44:45], v[50:51], v[44:45] op_sel:[1,0]
	v_pk_mul_f32 v[46:47], v[50:51], v[46:47] op_sel:[1,0]
	v_pk_mul_f32 v[40:41], v[50:51], v[40:41] op_sel:[1,0]
	v_pk_mul_f32 v[42:43], v[50:51], v[42:43] op_sel:[1,0]
	v_pk_fma_f32 v[34:35], v[82:83], v[34:35], v[14:15]
	v_pk_fma_f32 v[32:33], v[80:81], v[32:33], v[12:13]
	v_pk_fma_f32 v[38:39], v[10:11], v[38:39], v[86:87]
	v_pk_fma_f32 v[36:37], v[8:9], v[36:37], v[84:85]
	v_pk_fma_f32 v[10:11], v[10:11], v[46:47], v[86:87]
	v_pk_fma_f32 v[8:9], v[8:9], v[44:45], v[84:85]
	v_pk_fma_f32 v[14:15], v[82:83], v[42:43], v[14:15]
	v_pk_fma_f32 v[12:13], v[80:81], v[40:41], v[12:13]
	v_pk_mul_f32 v[32:33], v[32:33], s[18:19] op_sel_hi:[1,0]
	v_pk_mul_f32 v[34:35], v[34:35], s[18:19] op_sel_hi:[1,0]
	v_pk_mul_f32 v[36:37], v[36:37], s[18:19] op_sel_hi:[1,0]
	v_pk_mul_f32 v[38:39], v[38:39], s[18:19] op_sel_hi:[1,0]
	v_pk_mul_f32 v[8:9], v[8:9], s[18:19] op_sel_hi:[1,0]
	v_pk_mul_f32 v[10:11], v[10:11], s[18:19] op_sel_hi:[1,0]
	v_pk_mul_f32 v[12:13], v[12:13], s[18:19] op_sel_hi:[1,0]
	v_pk_mul_f32 v[14:15], v[14:15], s[18:19] op_sel_hi:[1,0]
	v_pk_fma_f32 v[30:31], v[30:31], v[6:7], v[34:35]
	v_pk_fma_f32 v[28:29], v[28:29], v[4:5], v[32:33]
	v_pk_fma_f32 v[26:27], v[26:27], v[2:3], v[38:39]
	v_pk_fma_f32 v[24:25], v[24:25], v[0:1], v[36:37]
	v_pk_fma_f32 v[10:11], v[18:19], v[2:3], v[10:11]
	v_pk_fma_f32 v[8:9], v[16:17], v[0:1], v[8:9]
	v_cvt_pk_bf16_f32 v0, v28, v29
	v_cvt_pk_bf16_f32 v1, v30, v31
	v_cvt_pk_bf16_f32 v2, v24, v25
	v_cvt_pk_bf16_f32 v3, v26, v27
	v_pk_fma_f32 v[6:7], v[22:23], v[6:7], v[14:15]
	v_pk_fma_f32 v[4:5], v[20:21], v[4:5], v[12:13]
	global_store_dwordx4 v[98:99], v[0:3], off offset:256
	s_nop 1
	v_cvt_pk_bf16_f32 v0, v4, v5
	v_cvt_pk_bf16_f32 v1, v6, v7
	v_cvt_pk_bf16_f32 v2, v8, v9
	v_cvt_pk_bf16_f32 v3, v10, v11
	global_store_dwordx4 v[96:97], v[0:3], off offset:256
	s_cbranch_vccz .LBB0_1105
	s_waitcnt vmcnt(0)
	s_cmpk_gt_u32 s19, 0xff
	s_cbranch_scc1 .LBB0_1116
	s_barrier
